# attn: VT staging loads moved from the EA phase to just after the feature barrier (ahead of the KF stream); VT written to LDS after the pre-loop MFMAs
# speedup vs baseline: 1.0056x; 1.0056x over previous
_Z11attn_kernelPKfS0_PKDF16_S0_S0_S0_S2_PDF16_S3_:
	s_load_dwordx16 s[4:19], s[0:1], 0x0
	s_load_dwordx2 s[62:63], s[0:1], 0x40
	v_readfirstlane_b32 s49, v0
	s_and_b32 s22, s2, 7
	s_lshr_b32 s23, s2, 3
	s_lshl_b32 s43, s22, 1
	s_and_b32 s24, s23, 1
	s_or_b32 s33, s43, s24
	s_lshr_b32 s41, s2, 4
	s_mul_i32 s41, s41, 24
	s_lshr_b32 s51, s49, 6
	s_mul_i32 s34, s33, 0xc0
	s_mov_b32 s35, 0
	s_lshl_b32 s25, s33, 5
	s_lshl_b32 s42, s22, 5
	s_add_i32 s42, s42, s23
	s_lshl_b32 s42, s42, 10
	s_add_i32 s36, s41, 23
	s_lshr_b32 s36, s36, 4
	s_and_b32 s36, s36, 0xffffffc
	s_lshr_b32 s37, s41, 4
	s_and_b32 s37, s37, 0xffffffc
	s_movk_i32 s40, 0x200
	v_lshrrev_b32_e32 v34, 5, v0
	v_bfe_u32 v35, v0, 1, 4
	v_mov_b32_e32 v115, 0
	v_lshlrev_b32_e32 v116, 4, v0
	v_add_u32_e32 v2, s41, v34
	v_lshrrev_b32_e32 v2, 1, v2
	v_mov_b32_e32 v3, v115
	v_lshl_add_u64 v[2:3], s[34:35], 0, v[2:3]
	v_lshlrev_b64 v[2:3], 9, v[2:3]
	v_lshlrev_b32_e32 v4, 5, v35
	v_mov_b32_e32 v5, v115
	v_lshrrev_b32_e32 v8, 3, v0
	v_and_b32_e32 v8, 4, v8
	v_mov_b32_e32 v9, v115
	v_lshrrev_b32_e32 v36, 2, v0
	s_movk_i32 s26, 0xab
	v_mul_u32_u24_e32 v36, s26, v36
	v_lshrrev_b32_e32 v36, 9, v36
	v_mul_u32_u24_e32 v37, 12, v36
	v_sub_u32_e32 v37, v0, v37
	s_lshl_b32 s27, s33, 6
	v_add_u32_e32 v38, s27, v36
	v_mul_u32_u24_e32 v38, 0x300, v38
	v_lshl_add_u32 v38, v37, 6, v38
	v_mul_u32_u24_e32 v39, 0x320, v36
	v_lshl_add_u32 v39, v37, 6, v39
	s_waitcnt lgkmcnt(0)
	s_add_u32 s26, s12, s25
	s_addc_u32 s27, s13, 0
	s_load_dword s52, s[26:27], s36 offset:0x0
	s_load_dword s53, s[26:27], s37 offset:0x0
	s_load_dwordx4 s[56:59], s[12:13], s25 offset:0x200
	s_load_dwordx2 s[60:61], s[12:13], s25 offset:0x210
	s_load_dwordx2 s[28:29], s[12:13], 0x400
	v_lshl_add_u64 v[2:3], s[4:5], 0, v[2:3]
	v_lshl_add_u64 v[6:7], v[2:3], 0, v[4:5]
	v_lshlrev_b32_e32 v2, 4, v35
	v_lshl_add_u64 v[10:11], v[6:7], 0, v[8:9]
	global_load_dwordx4 v[2:5], v2, s[10:11]
	s_nop 0
	global_load_dword v8, v[10:11], off offset:24
	global_load_dword v6, v[10:11], off
	global_load_dword v7, v[10:11], off offset:8
	global_load_dword v9, v[10:11], off offset:16
	s_waitcnt lgkmcnt(0)
	v_max_f32_e64 v10, s52, s52
	v_max_f32_e64 v11, s53, s53
	v_max_f32_e32 v10, v11, v10
	v_max_f32_e64 v11, s57, s57
	v_max_f32_e64 v12, s56, s56
	v_max_f32_e32 v11, v12, v11
	v_max_f32_e64 v12, s59, s59
	v_max_f32_e64 v13, s58, s58
	v_max_f32_e32 v12, v13, v12
	v_max_f32_e64 v13, s61, s61
	v_max_f32_e64 v14, s60, s60
	v_max_f32_e32 v13, v14, v13
	v_max3_f32 v11, v11, v12, v13
	s_mov_b32 s24, 0x41700000
	v_cmp_gt_f32_e32 vcc, s24, v10
	v_cmp_gt_f32_e64 s[26:27], s24, v11
	s_and_b64 s[26:27], vcc, s[26:27]
	v_cmp_lt_f32_e64 s[36:37], s29, 4.0
	s_and_b64 s[26:27], s[26:27], s[36:37]
	v_max_f32_e32 v12, v10, v10
	v_max_f32_e32 v12, 1.0, v12
	v_mul_f32_e32 v13, v12, v12
	v_mul_f32_e32 v13, v12, v13
	v_mul_f32_e32 v12, v12, v13
	v_mul_f32_e32 v12, s29, v12
	s_mov_b32 s24, 0x476a6000
	v_cmp_gt_f32_e64 s[36:37], s24, v12
	s_and_b64 s[26:27], s[26:27], s[36:37]
	s_andn2_b64 vcc, exec, s[26:27]
	s_cbranch_vccz .Lf_fast
	s_waitcnt vmcnt(0)
	s_branch .Lattn_orig

.Lf_27:
	s_or_b64 exec, exec, s[2:3]
	v_and_b32_e32 v2, 0x3f0, v116
	v_add_u32_e32 v166, 0, v2
	s_waitcnt lgkmcnt(0)
	s_barrier
	global_load_dwordx4 v[66:69], v38, s[8:9]
	global_load_dwordx4 v[70:73], v38, s[8:9] offset:16
	global_load_dwordx4 v[74:77], v38, s[8:9] offset:32
	global_load_dwordx4 v[78:81], v38, s[8:9] offset:48
	v_and_b32_e32 v167, 31, v0
	v_lshl_or_b32 v167, s51, 5, v167
	s_mul_i32 s38, s33, 0x1800
	v_add_u32_e32 v2, s38, v167
	v_lshlrev_b32_e32 v2, 5, v2
	v_bfe_u32 v3, v0, 5, 1
	v_lshl_add_u32 v2, v3, 4, v2
	s_mov_b32 s44, s16
	s_mov_b32 s45, s17
	global_load_dwordx4 v[102:105], v2, s[44:45]
	s_add_u32 s44, s44, 0x3000
	s_addc_u32 s45, s45, 0
	global_load_dwordx4 v[106:109], v2, s[44:45]
	s_add_u32 s44, s44, 0x3000
	s_addc_u32 s45, s45, 0
	global_load_dwordx4 v[110:113], v2, s[44:45]
	s_add_u32 s44, s44, 0x3000
	s_addc_u32 s45, s45, 0
	global_load_dwordx4 v[114:117], v2, s[44:45]
	s_add_u32 s44, s44, 0x3000
	s_addc_u32 s45, s45, 0
	global_load_dwordx4 v[118:121], v2, s[44:45]
	s_add_u32 s44, s44, 0x3000
	s_addc_u32 s45, s45, 0
	global_load_dwordx4 v[122:125], v2, s[44:45]
	s_add_u32 s44, s44, 0x3000
	s_addc_u32 s45, s45, 0
	global_load_dwordx4 v[126:129], v2, s[44:45]
	s_add_u32 s44, s44, 0x3000
	s_addc_u32 s45, s45, 0
	global_load_dwordx4 v[130:133], v2, s[44:45]
	s_add_u32 s44, s44, 0x3000
	s_addc_u32 s45, s45, 0
	global_load_dwordx4 v[134:137], v2, s[44:45]
	s_add_u32 s44, s44, 0x3000
	s_addc_u32 s45, s45, 0
	global_load_dwordx4 v[138:141], v2, s[44:45]
	s_add_u32 s44, s44, 0x3000
	s_addc_u32 s45, s45, 0
	global_load_dwordx4 v[142:145], v2, s[44:45]
	s_add_u32 s44, s44, 0x3000
	s_addc_u32 s45, s45, 0
	global_load_dwordx4 v[146:149], v2, s[44:45]
	s_add_u32 s44, s44, 0x3000
	s_addc_u32 s45, s45, 0
	global_load_dwordx4 v[150:153], v2, s[44:45]
	s_add_u32 s44, s44, 0x3000
	s_addc_u32 s45, s45, 0
	global_load_dwordx4 v[154:157], v2, s[44:45]
	s_add_u32 s44, s44, 0x3000
	s_addc_u32 s45, s45, 0
	global_load_dwordx4 v[158:161], v2, s[44:45]
	s_add_u32 s44, s44, 0x3000
	s_addc_u32 s45, s45, 0
	global_load_dwordx4 v[162:165], v2, s[44:45]
	v_mul_u32_u24_e32 v1, 0xc40, v3
	v_lshl_add_u32 v1, v167, 1, v1
	v_add_u32_e32 v1, 0x18000, v1
	v_mov_b32_e32 v167, v39
	v_mov_b32_e32 v90, 0
	v_mov_b32_e32 v91, 0
	v_mov_b32_e32 v92, 0
	v_mov_b32_e32 v93, 0
	v_mov_b32_e32 v94, 0
	v_mov_b32_e32 v95, 0
	v_mov_b32_e32 v96, 0
	v_mov_b32_e32 v97, 0
	v_mov_b32_e32 v98, 0
	v_mov_b32_e32 v99, 0
	v_mov_b32_e32 v100, 0
	v_mov_b32_e32 v101, 0
	ds_read_b128 v[46:49], v166 offset:2048
	ds_read_b128 v[14:17], v166 offset:0
	ds_read_b128 v[30:33], v166 offset:1024
	ds_read_b128 v[62:65], v166 offset:3072
	s_waitcnt vmcnt(14) lgkmcnt(3)
	v_mfma_f32_32x32x16_f16 v[34:49], v[46:49], v[106:109], 0
	s_waitcnt lgkmcnt(2)
	v_mfma_f32_32x32x16_f16 v[2:17], v[14:17], v[102:105], 0
	s_waitcnt lgkmcnt(1)
	v_mfma_f32_32x32x16_f16 v[18:33], v[30:33], v[102:105], 0
	s_waitcnt lgkmcnt(0)
	v_mfma_f32_32x32x16_f16 v[50:65], v[62:65], v[106:109], 0
	ds_write_b128 v167, v[66:69] offset:32768
	ds_write_b128 v167, v[70:73] offset:32784
	ds_write_b128 v167, v[74:77] offset:32800
	ds_write_b128 v167, v[78:81] offset:32816
	s_lshl_b32 s22, s42, 2
	s_cmpk_lt_u32 s49, 0x100
	s_cselect_b32 s20, s14, s10
	s_cselect_b32 s21, s15, s11
	s_cselect_b32 s22, s22, 0
	s_cselect_b32 s23, 0xff, 15
	v_and_b32_e32 v82, s23, v0
	v_lshlrev_b32_e32 v82, 4, v82
	v_add_u32_e32 v82, s22, v82
	global_load_dwordx4 v[102:105], v82, s[20:21]
	s_nop 7
	ds_read_b128 v[46:49], v166 offset:6144
	ds_read_b128 v[14:17], v166 offset:4096
	ds_read_b128 v[30:33], v166 offset:5120
	ds_read_b128 v[62:65], v166 offset:7168
	v_pk_mul_f32 v[66:67], v[34:35], v[18:19]
	v_pk_mul_f32 v[68:69], v[36:37], v[20:21]
	v_pk_mul_f32 v[70:71], v[38:39], v[22:23]
	v_pk_mul_f32 v[72:73], v[40:41], v[24:25]
	v_pk_mul_f32 v[74:75], v[42:43], v[26:27]
	v_pk_mul_f32 v[76:77], v[44:45], v[28:29]
	s_waitcnt vmcnt(13) lgkmcnt(3)
	v_mfma_f32_32x32x16_f16 v[34:49], v[46:49], v[114:117], 0
	v_pk_fma_f32 v[66:67], v[2:3], v[50:51], v[66:67]
	v_pk_fma_f32 v[68:69], v[4:5], v[52:53], v[68:69]
	v_pk_fma_f32 v[70:71], v[6:7], v[54:55], v[70:71]
	v_pk_fma_f32 v[72:73], v[8:9], v[56:57], v[72:73]
	v_pk_fma_f32 v[74:75], v[10:11], v[58:59], v[74:75]
	v_pk_fma_f32 v[76:77], v[12:13], v[60:61], v[76:77]
	s_waitcnt lgkmcnt(2)
	v_mfma_f32_32x32x16_f16 v[2:17], v[14:17], v[110:113], 0
	v_pk_mul_f32 v[78:79], v[18:19], v[50:51]
	v_pk_mul_f32 v[80:81], v[20:21], v[52:53]
	v_pk_mul_f32 v[82:83], v[22:23], v[54:55]
	v_pk_mul_f32 v[84:85], v[24:25], v[56:57]
	v_pk_mul_f32 v[86:87], v[26:27], v[58:59]
	v_pk_mul_f32 v[88:89], v[28:29], v[60:61]
	s_waitcnt lgkmcnt(1)
	v_mfma_f32_32x32x16_f16 v[18:33], v[30:33], v[110:113], 0
	s_waitcnt lgkmcnt(0)
	v_mfma_f32_32x32x16_f16 v[50:65], v[62:65], v[114:117], 0
	v_rcp_f32_e32 v78, v78
	v_rcp_f32_e32 v79, v79
	v_rcp_f32_e32 v80, v80
	v_rcp_f32_e32 v81, v81
	v_rcp_f32_e32 v82, v82
	v_rcp_f32_e32 v83, v83
	v_rcp_f32_e32 v84, v84
	v_rcp_f32_e32 v85, v85
	v_rcp_f32_e32 v86, v86
	v_rcp_f32_e32 v87, v87
	v_rcp_f32_e32 v88, v88
	v_rcp_f32_e32 v89, v89
	v_pk_fma_f32 v[90:91], v[66:67], v[78:79], v[90:91]
	v_pk_fma_f32 v[92:93], v[68:69], v[80:81], v[92:93]
	v_pk_fma_f32 v[94:95], v[70:71], v[82:83], v[94:95]
	v_pk_fma_f32 v[96:97], v[72:73], v[84:85], v[96:97]
	v_pk_fma_f32 v[98:99], v[74:75], v[86:87], v[98:99]
	v_pk_fma_f32 v[100:101], v[76:77], v[88:89], v[100:101]
	ds_read_b128 v[46:49], v166 offset:10240
	ds_read_b128 v[14:17], v166 offset:8192
	ds_read_b128 v[30:33], v166 offset:9216
	ds_read_b128 v[62:65], v166 offset:11264
	v_pk_mul_f32 v[66:67], v[34:35], v[18:19]
	v_pk_mul_f32 v[68:69], v[36:37], v[20:21]
	v_pk_mul_f32 v[70:71], v[38:39], v[22:23]
	v_pk_mul_f32 v[72:73], v[40:41], v[24:25]
	v_pk_mul_f32 v[74:75], v[42:43], v[26:27]
	v_pk_mul_f32 v[76:77], v[44:45], v[28:29]
	s_waitcnt vmcnt(11) lgkmcnt(3)
	v_mfma_f32_32x32x16_f16 v[34:49], v[46:49], v[122:125], 0
	v_pk_fma_f32 v[66:67], v[2:3], v[50:51], v[66:67]
	v_pk_fma_f32 v[68:69], v[4:5], v[52:53], v[68:69]
	v_pk_fma_f32 v[70:71], v[6:7], v[54:55], v[70:71]
	v_pk_fma_f32 v[72:73], v[8:9], v[56:57], v[72:73]
	v_pk_fma_f32 v[74:75], v[10:11], v[58:59], v[74:75]
	v_pk_fma_f32 v[76:77], v[12:13], v[60:61], v[76:77]
	s_waitcnt lgkmcnt(2)
	v_mfma_f32_32x32x16_f16 v[2:17], v[14:17], v[118:121], 0
	v_pk_mul_f32 v[78:79], v[18:19], v[50:51]
	v_pk_mul_f32 v[80:81], v[20:21], v[52:53]
	v_pk_mul_f32 v[82:83], v[22:23], v[54:55]
	v_pk_mul_f32 v[84:85], v[24:25], v[56:57]
	v_pk_mul_f32 v[86:87], v[26:27], v[58:59]
	v_pk_mul_f32 v[88:89], v[28:29], v[60:61]
	s_waitcnt lgkmcnt(1)
	v_mfma_f32_32x32x16_f16 v[18:33], v[30:33], v[118:121], 0
	s_waitcnt lgkmcnt(0)
	v_mfma_f32_32x32x16_f16 v[50:65], v[62:65], v[122:125], 0
	v_rcp_f32_e32 v78, v78
	v_rcp_f32_e32 v79, v79
	v_rcp_f32_e32 v80, v80
	v_rcp_f32_e32 v81, v81
	v_rcp_f32_e32 v82, v82
	v_rcp_f32_e32 v83, v83
	v_rcp_f32_e32 v84, v84
	v_rcp_f32_e32 v85, v85
	v_rcp_f32_e32 v86, v86
	v_rcp_f32_e32 v87, v87
	v_rcp_f32_e32 v88, v88
	v_rcp_f32_e32 v89, v89
	v_pk_fma_f32 v[90:91], v[66:67], v[78:79], v[90:91]
	v_pk_fma_f32 v[92:93], v[68:69], v[80:81], v[92:93]
	v_pk_fma_f32 v[94:95], v[70:71], v[82:83], v[94:95]
	v_pk_fma_f32 v[96:97], v[72:73], v[84:85], v[96:97]
	v_pk_fma_f32 v[98:99], v[74:75], v[86:87], v[98:99]
	v_pk_fma_f32 v[100:101], v[76:77], v[88:89], v[100:101]
	ds_read_b128 v[46:49], v166 offset:14336
	ds_read_b128 v[14:17], v166 offset:12288
	ds_read_b128 v[30:33], v166 offset:13312
	ds_read_b128 v[62:65], v166 offset:15360
	v_pk_mul_f32 v[66:67], v[34:35], v[18:19]
	v_pk_mul_f32 v[68:69], v[36:37], v[20:21]
	v_pk_mul_f32 v[70:71], v[38:39], v[22:23]
	v_pk_mul_f32 v[72:73], v[40:41], v[24:25]
	v_pk_mul_f32 v[74:75], v[42:43], v[26:27]
	v_pk_mul_f32 v[76:77], v[44:45], v[28:29]
	s_waitcnt vmcnt(9) lgkmcnt(3)
	v_mfma_f32_32x32x16_f16 v[34:49], v[46:49], v[130:133], 0
	v_pk_fma_f32 v[66:67], v[2:3], v[50:51], v[66:67]
	v_pk_fma_f32 v[68:69], v[4:5], v[52:53], v[68:69]
	v_pk_fma_f32 v[70:71], v[6:7], v[54:55], v[70:71]
	v_pk_fma_f32 v[72:73], v[8:9], v[56:57], v[72:73]
	v_pk_fma_f32 v[74:75], v[10:11], v[58:59], v[74:75]
	v_pk_fma_f32 v[76:77], v[12:13], v[60:61], v[76:77]
	s_waitcnt lgkmcnt(2)
	v_mfma_f32_32x32x16_f16 v[2:17], v[14:17], v[126:129], 0
	v_pk_mul_f32 v[78:79], v[18:19], v[50:51]
	v_pk_mul_f32 v[80:81], v[20:21], v[52:53]
	v_pk_mul_f32 v[82:83], v[22:23], v[54:55]
	v_pk_mul_f32 v[84:85], v[24:25], v[56:57]
	v_pk_mul_f32 v[86:87], v[26:27], v[58:59]
	v_pk_mul_f32 v[88:89], v[28:29], v[60:61]
	s_waitcnt lgkmcnt(1)
	v_mfma_f32_32x32x16_f16 v[18:33], v[30:33], v[126:129], 0
	s_waitcnt lgkmcnt(0)
	v_mfma_f32_32x32x16_f16 v[50:65], v[62:65], v[130:133], 0
	v_rcp_f32_e32 v78, v78
	v_rcp_f32_e32 v79, v79
	v_rcp_f32_e32 v80, v80
	v_rcp_f32_e32 v81, v81
	v_rcp_f32_e32 v82, v82
	v_rcp_f32_e32 v83, v83
	v_rcp_f32_e32 v84, v84
	v_rcp_f32_e32 v85, v85
	v_rcp_f32_e32 v86, v86
	v_rcp_f32_e32 v87, v87
	v_rcp_f32_e32 v88, v88
	v_rcp_f32_e32 v89, v89
	v_pk_fma_f32 v[90:91], v[66:67], v[78:79], v[90:91]
	v_pk_fma_f32 v[92:93], v[68:69], v[80:81], v[92:93]
	v_pk_fma_f32 v[94:95], v[70:71], v[82:83], v[94:95]
	v_pk_fma_f32 v[96:97], v[72:73], v[84:85], v[96:97]
	v_pk_fma_f32 v[98:99], v[74:75], v[86:87], v[98:99]
	v_pk_fma_f32 v[100:101], v[76:77], v[88:89], v[100:101]
	ds_read_b128 v[46:49], v166 offset:18432
	ds_read_b128 v[14:17], v166 offset:16384
	ds_read_b128 v[30:33], v166 offset:17408
	ds_read_b128 v[62:65], v166 offset:19456
	v_pk_mul_f32 v[66:67], v[34:35], v[18:19]
	v_pk_mul_f32 v[68:69], v[36:37], v[20:21]
	v_pk_mul_f32 v[70:71], v[38:39], v[22:23]
	v_pk_mul_f32 v[72:73], v[40:41], v[24:25]
	v_pk_mul_f32 v[74:75], v[42:43], v[26:27]
	v_pk_mul_f32 v[76:77], v[44:45], v[28:29]
	s_waitcnt vmcnt(7) lgkmcnt(3)
	v_mfma_f32_32x32x16_f16 v[34:49], v[46:49], v[138:141], 0
	v_pk_fma_f32 v[66:67], v[2:3], v[50:51], v[66:67]
	v_pk_fma_f32 v[68:69], v[4:5], v[52:53], v[68:69]
	v_pk_fma_f32 v[70:71], v[6:7], v[54:55], v[70:71]
	v_pk_fma_f32 v[72:73], v[8:9], v[56:57], v[72:73]
	v_pk_fma_f32 v[74:75], v[10:11], v[58:59], v[74:75]
	v_pk_fma_f32 v[76:77], v[12:13], v[60:61], v[76:77]
	s_waitcnt lgkmcnt(2)
	v_mfma_f32_32x32x16_f16 v[2:17], v[14:17], v[134:137], 0
	v_pk_mul_f32 v[78:79], v[18:19], v[50:51]
	v_pk_mul_f32 v[80:81], v[20:21], v[52:53]
	v_pk_mul_f32 v[82:83], v[22:23], v[54:55]
	v_pk_mul_f32 v[84:85], v[24:25], v[56:57]
	v_pk_mul_f32 v[86:87], v[26:27], v[58:59]
	v_pk_mul_f32 v[88:89], v[28:29], v[60:61]
	s_waitcnt lgkmcnt(1)
	v_mfma_f32_32x32x16_f16 v[18:33], v[30:33], v[134:137], 0
	s_waitcnt lgkmcnt(0)
	v_mfma_f32_32x32x16_f16 v[50:65], v[62:65], v[138:141], 0
	v_rcp_f32_e32 v78, v78
	v_rcp_f32_e32 v79, v79
	v_rcp_f32_e32 v80, v80
	v_rcp_f32_e32 v81, v81
	v_rcp_f32_e32 v82, v82
	v_rcp_f32_e32 v83, v83
	v_rcp_f32_e32 v84, v84
	v_rcp_f32_e32 v85, v85
	v_rcp_f32_e32 v86, v86
	v_rcp_f32_e32 v87, v87
	v_rcp_f32_e32 v88, v88
	v_rcp_f32_e32 v89, v89
	v_pk_fma_f32 v[90:91], v[66:67], v[78:79], v[90:91]
	v_pk_fma_f32 v[92:93], v[68:69], v[80:81], v[92:93]
	v_pk_fma_f32 v[94:95], v[70:71], v[82:83], v[94:95]
	v_pk_fma_f32 v[96:97], v[72:73], v[84:85], v[96:97]
	v_pk_fma_f32 v[98:99], v[74:75], v[86:87], v[98:99]
	v_pk_fma_f32 v[100:101], v[76:77], v[88:89], v[100:101]
	ds_read_b128 v[46:49], v166 offset:22528
	ds_read_b128 v[14:17], v166 offset:20480
	ds_read_b128 v[30:33], v166 offset:21504
	ds_read_b128 v[62:65], v166 offset:23552
	v_pk_mul_f32 v[66:67], v[34:35], v[18:19]
	v_pk_mul_f32 v[68:69], v[36:37], v[20:21]
	v_pk_mul_f32 v[70:71], v[38:39], v[22:23]
	v_pk_mul_f32 v[72:73], v[40:41], v[24:25]
	v_pk_mul_f32 v[74:75], v[42:43], v[26:27]
	v_pk_mul_f32 v[76:77], v[44:45], v[28:29]
	s_waitcnt vmcnt(5) lgkmcnt(3)
	v_mfma_f32_32x32x16_f16 v[34:49], v[46:49], v[146:149], 0
	v_pk_fma_f32 v[66:67], v[2:3], v[50:51], v[66:67]
	v_pk_fma_f32 v[68:69], v[4:5], v[52:53], v[68:69]
	v_pk_fma_f32 v[70:71], v[6:7], v[54:55], v[70:71]
	v_pk_fma_f32 v[72:73], v[8:9], v[56:57], v[72:73]
	v_pk_fma_f32 v[74:75], v[10:11], v[58:59], v[74:75]
	v_pk_fma_f32 v[76:77], v[12:13], v[60:61], v[76:77]
	s_waitcnt lgkmcnt(2)
	v_mfma_f32_32x32x16_f16 v[2:17], v[14:17], v[142:145], 0
	v_pk_mul_f32 v[78:79], v[18:19], v[50:51]
	v_pk_mul_f32 v[80:81], v[20:21], v[52:53]
	v_pk_mul_f32 v[82:83], v[22:23], v[54:55]
	v_pk_mul_f32 v[84:85], v[24:25], v[56:57]
	v_pk_mul_f32 v[86:87], v[26:27], v[58:59]
	v_pk_mul_f32 v[88:89], v[28:29], v[60:61]
	s_waitcnt lgkmcnt(1)
	v_mfma_f32_32x32x16_f16 v[18:33], v[30:33], v[142:145], 0
	s_waitcnt lgkmcnt(0)
	v_mfma_f32_32x32x16_f16 v[50:65], v[62:65], v[146:149], 0
	v_rcp_f32_e32 v78, v78
	v_rcp_f32_e32 v79, v79
	v_rcp_f32_e32 v80, v80
	v_rcp_f32_e32 v81, v81
	v_rcp_f32_e32 v82, v82
	v_rcp_f32_e32 v83, v83
	v_rcp_f32_e32 v84, v84
	v_rcp_f32_e32 v85, v85
	v_rcp_f32_e32 v86, v86
	v_rcp_f32_e32 v87, v87
	v_rcp_f32_e32 v88, v88
	v_rcp_f32_e32 v89, v89
	v_pk_fma_f32 v[90:91], v[66:67], v[78:79], v[90:91]
	v_pk_fma_f32 v[92:93], v[68:69], v[80:81], v[92:93]
	v_pk_fma_f32 v[94:95], v[70:71], v[82:83], v[94:95]
	v_pk_fma_f32 v[96:97], v[72:73], v[84:85], v[96:97]
	v_pk_fma_f32 v[98:99], v[74:75], v[86:87], v[98:99]
	v_pk_fma_f32 v[100:101], v[76:77], v[88:89], v[100:101]
	ds_read_b128 v[46:49], v166 offset:26624
	ds_read_b128 v[14:17], v166 offset:24576
	ds_read_b128 v[30:33], v166 offset:25600
	ds_read_b128 v[62:65], v166 offset:27648
	v_pk_mul_f32 v[66:67], v[34:35], v[18:19]
	v_pk_mul_f32 v[68:69], v[36:37], v[20:21]
	v_pk_mul_f32 v[70:71], v[38:39], v[22:23]
	v_pk_mul_f32 v[72:73], v[40:41], v[24:25]
	v_pk_mul_f32 v[74:75], v[42:43], v[26:27]
	v_pk_mul_f32 v[76:77], v[44:45], v[28:29]
	s_waitcnt vmcnt(3) lgkmcnt(3)
	v_mfma_f32_32x32x16_f16 v[34:49], v[46:49], v[154:157], 0
	v_pk_fma_f32 v[66:67], v[2:3], v[50:51], v[66:67]
	v_pk_fma_f32 v[68:69], v[4:5], v[52:53], v[68:69]
	v_pk_fma_f32 v[70:71], v[6:7], v[54:55], v[70:71]
	v_pk_fma_f32 v[72:73], v[8:9], v[56:57], v[72:73]
	v_pk_fma_f32 v[74:75], v[10:11], v[58:59], v[74:75]
	v_pk_fma_f32 v[76:77], v[12:13], v[60:61], v[76:77]
	s_waitcnt lgkmcnt(2)
	v_mfma_f32_32x32x16_f16 v[2:17], v[14:17], v[150:153], 0
	v_pk_mul_f32 v[78:79], v[18:19], v[50:51]
	v_pk_mul_f32 v[80:81], v[20:21], v[52:53]
	v_pk_mul_f32 v[82:83], v[22:23], v[54:55]
	v_pk_mul_f32 v[84:85], v[24:25], v[56:57]
	v_pk_mul_f32 v[86:87], v[26:27], v[58:59]
	v_pk_mul_f32 v[88:89], v[28:29], v[60:61]
	s_waitcnt lgkmcnt(1)
	v_mfma_f32_32x32x16_f16 v[18:33], v[30:33], v[150:153], 0
	s_waitcnt lgkmcnt(0)
	v_mfma_f32_32x32x16_f16 v[50:65], v[62:65], v[154:157], 0
	v_rcp_f32_e32 v78, v78
	v_rcp_f32_e32 v79, v79
	v_rcp_f32_e32 v80, v80
	v_rcp_f32_e32 v81, v81
	v_rcp_f32_e32 v82, v82
	v_rcp_f32_e32 v83, v83
	v_rcp_f32_e32 v84, v84
	v_rcp_f32_e32 v85, v85
	v_rcp_f32_e32 v86, v86
	v_rcp_f32_e32 v87, v87
	v_rcp_f32_e32 v88, v88
	v_rcp_f32_e32 v89, v89
	v_pk_fma_f32 v[90:91], v[66:67], v[78:79], v[90:91]
	v_pk_fma_f32 v[92:93], v[68:69], v[80:81], v[92:93]
	v_pk_fma_f32 v[94:95], v[70:71], v[82:83], v[94:95]
	v_pk_fma_f32 v[96:97], v[72:73], v[84:85], v[96:97]
	v_pk_fma_f32 v[98:99], v[74:75], v[86:87], v[98:99]
	v_pk_fma_f32 v[100:101], v[76:77], v[88:89], v[100:101]
	ds_read_b128 v[46:49], v166 offset:30720
	ds_read_b128 v[14:17], v166 offset:28672
	ds_read_b128 v[30:33], v166 offset:29696
	ds_read_b128 v[62:65], v166 offset:31744
	v_pk_mul_f32 v[66:67], v[34:35], v[18:19]
	v_pk_mul_f32 v[68:69], v[36:37], v[20:21]
	v_pk_mul_f32 v[70:71], v[38:39], v[22:23]
	v_pk_mul_f32 v[72:73], v[40:41], v[24:25]
	v_pk_mul_f32 v[74:75], v[42:43], v[26:27]
	v_pk_mul_f32 v[76:77], v[44:45], v[28:29]
	s_waitcnt vmcnt(1) lgkmcnt(3)
	v_mfma_f32_32x32x16_f16 v[34:49], v[46:49], v[162:165], 0
	v_pk_fma_f32 v[66:67], v[2:3], v[50:51], v[66:67]
	v_pk_fma_f32 v[68:69], v[4:5], v[52:53], v[68:69]
	v_pk_fma_f32 v[70:71], v[6:7], v[54:55], v[70:71]
	v_pk_fma_f32 v[72:73], v[8:9], v[56:57], v[72:73]
	v_pk_fma_f32 v[74:75], v[10:11], v[58:59], v[74:75]
	v_pk_fma_f32 v[76:77], v[12:13], v[60:61], v[76:77]
	s_waitcnt lgkmcnt(2)
	v_mfma_f32_32x32x16_f16 v[2:17], v[14:17], v[158:161], 0
	v_pk_mul_f32 v[78:79], v[18:19], v[50:51]
	v_pk_mul_f32 v[80:81], v[20:21], v[52:53]
	v_pk_mul_f32 v[82:83], v[22:23], v[54:55]
	v_pk_mul_f32 v[84:85], v[24:25], v[56:57]
	v_pk_mul_f32 v[86:87], v[26:27], v[58:59]
	v_pk_mul_f32 v[88:89], v[28:29], v[60:61]
	s_waitcnt lgkmcnt(1)
	v_mfma_f32_32x32x16_f16 v[18:33], v[30:33], v[158:161], 0
	s_waitcnt lgkmcnt(0)
	v_mfma_f32_32x32x16_f16 v[50:65], v[62:65], v[162:165], 0
	v_rcp_f32_e32 v78, v78
	v_rcp_f32_e32 v79, v79
	v_rcp_f32_e32 v80, v80
	v_rcp_f32_e32 v81, v81
	v_rcp_f32_e32 v82, v82
	v_rcp_f32_e32 v83, v83
	v_rcp_f32_e32 v84, v84
	v_rcp_f32_e32 v85, v85
	v_rcp_f32_e32 v86, v86
	v_rcp_f32_e32 v87, v87
	v_rcp_f32_e32 v88, v88
	v_rcp_f32_e32 v89, v89
	v_pk_fma_f32 v[90:91], v[66:67], v[78:79], v[90:91]
	v_pk_fma_f32 v[92:93], v[68:69], v[80:81], v[92:93]
	v_pk_fma_f32 v[94:95], v[70:71], v[82:83], v[94:95]
	v_pk_fma_f32 v[96:97], v[72:73], v[84:85], v[96:97]
	v_pk_fma_f32 v[98:99], v[74:75], v[86:87], v[98:99]
	v_pk_fma_f32 v[100:101], v[76:77], v[88:89], v[100:101]
	v_pk_mul_f32 v[66:67], v[34:35], v[18:19]
	v_pk_mul_f32 v[68:69], v[36:37], v[20:21]
	v_pk_mul_f32 v[70:71], v[38:39], v[22:23]
	v_pk_mul_f32 v[72:73], v[40:41], v[24:25]
	v_pk_mul_f32 v[74:75], v[42:43], v[26:27]
	v_pk_mul_f32 v[76:77], v[44:45], v[28:29]
	v_pk_fma_f32 v[66:67], v[2:3], v[50:51], v[66:67]
	v_pk_fma_f32 v[68:69], v[4:5], v[52:53], v[68:69]
	v_pk_fma_f32 v[70:71], v[6:7], v[54:55], v[70:71]
	v_pk_fma_f32 v[72:73], v[8:9], v[56:57], v[72:73]
	v_pk_fma_f32 v[74:75], v[10:11], v[58:59], v[74:75]
	v_pk_fma_f32 v[76:77], v[12:13], v[60:61], v[76:77]
	v_pk_mul_f32 v[78:79], v[18:19], v[50:51]
	v_pk_mul_f32 v[80:81], v[20:21], v[52:53]
	v_pk_mul_f32 v[82:83], v[22:23], v[54:55]
	v_pk_mul_f32 v[84:85], v[24:25], v[56:57]
	v_pk_mul_f32 v[86:87], v[26:27], v[58:59]
	v_pk_mul_f32 v[88:89], v[28:29], v[60:61]
	v_rcp_f32_e32 v78, v78
	v_rcp_f32_e32 v79, v79
	v_rcp_f32_e32 v80, v80
	v_rcp_f32_e32 v81, v81
	v_rcp_f32_e32 v82, v82
	v_rcp_f32_e32 v83, v83
	v_rcp_f32_e32 v84, v84
	v_rcp_f32_e32 v85, v85
	v_rcp_f32_e32 v86, v86
	v_rcp_f32_e32 v87, v87
	v_rcp_f32_e32 v88, v88
	v_rcp_f32_e32 v89, v89
	v_pk_fma_f32 v[90:91], v[66:67], v[78:79], v[90:91]
	v_pk_fma_f32 v[92:93], v[68:69], v[80:81], v[92:93]
	v_pk_fma_f32 v[94:95], v[70:71], v[82:83], v[94:95]
	v_pk_fma_f32 v[96:97], v[72:73], v[84:85], v[96:97]
	v_pk_fma_f32 v[98:99], v[74:75], v[86:87], v[98:99]
	v_pk_fma_f32 v[100:101], v[76:77], v[88:89], v[100:101]
	v_fma_f32 v66, v90, -2.0, s28
	v_subrev_f32_e32 v66, s29, v66
	v_mul_f32_e32 v66, 0x3fb8aa3b, v66
	v_exp_f32_e32 v66, v66
	v_fma_f32 v67, v91, -2.0, s28
	v_subrev_f32_e32 v67, s29, v67
	v_mul_f32_e32 v67, 0x3fb8aa3b, v67
	v_exp_f32_e32 v67, v67
	v_fma_f32 v68, v92, -2.0, s28
	v_subrev_f32_e32 v68, s29, v68
	v_mul_f32_e32 v68, 0x3fb8aa3b, v68
	v_exp_f32_e32 v68, v68
	v_fma_f32 v69, v93, -2.0, s28
	v_subrev_f32_e32 v69, s29, v69
	v_mul_f32_e32 v69, 0x3fb8aa3b, v69
	v_exp_f32_e32 v69, v69
	v_fma_f32 v70, v94, -2.0, s28
	v_subrev_f32_e32 v70, s29, v70
	v_mul_f32_e32 v70, 0x3fb8aa3b, v70
	v_exp_f32_e32 v70, v70
	v_fma_f32 v71, v95, -2.0, s28
	v_subrev_f32_e32 v71, s29, v71
	v_mul_f32_e32 v71, 0x3fb8aa3b, v71
	v_exp_f32_e32 v71, v71
	v_fma_f32 v72, v96, -2.0, s28
	v_subrev_f32_e32 v72, s29, v72
	v_mul_f32_e32 v72, 0x3fb8aa3b, v72
	v_exp_f32_e32 v72, v72
	v_fma_f32 v73, v97, -2.0, s28
	v_subrev_f32_e32 v73, s29, v73
	v_mul_f32_e32 v73, 0x3fb8aa3b, v73
	v_exp_f32_e32 v73, v73
	v_fma_f32 v74, v98, -2.0, s28
	v_subrev_f32_e32 v74, s29, v74
	v_mul_f32_e32 v74, 0x3fb8aa3b, v74
	v_exp_f32_e32 v74, v74
	v_fma_f32 v75, v99, -2.0, s28
	v_subrev_f32_e32 v75, s29, v75
	v_mul_f32_e32 v75, 0x3fb8aa3b, v75
	v_exp_f32_e32 v75, v75
	v_fma_f32 v76, v100, -2.0, s28
	v_subrev_f32_e32 v76, s29, v76
	v_mul_f32_e32 v76, 0x3fb8aa3b, v76
	v_exp_f32_e32 v76, v76
	v_fma_f32 v77, v101, -2.0, s28
	v_subrev_f32_e32 v77, s29, v77
	v_mul_f32_e32 v77, 0x3fb8aa3b, v77
	v_exp_f32_e32 v77, v77
	s_nop 0
	v_cvt_f16_f32_e32 v66, v66
	v_cvt_f16_f32_e32 v67, v67
	v_cvt_f16_f32_e32 v68, v68
	v_cvt_f16_f32_e32 v69, v69
	v_cvt_f16_f32_e32 v70, v70
	v_cvt_f16_f32_e32 v71, v71
	v_cvt_f16_f32_e32 v72, v72
	v_cvt_f16_f32_e32 v73, v73
	v_cvt_f16_f32_e32 v74, v74
	v_cvt_f16_f32_e32 v75, v75
	v_cvt_f16_f32_e32 v76, v76
	v_cvt_f16_f32_e32 v77, v77
	ds_write_b16 v1, v66
	ds_write_b16 v1, v67 offset:784
	ds_write_b16 v1, v68 offset:1568
	ds_write_b16 v1, v69 offset:2352
	ds_write_b16 v1, v70 offset:6272
	ds_write_b16 v1, v71 offset:7056
	ds_write_b16 v1, v72 offset:7840
	ds_write_b16 v1, v73 offset:8624
	ds_write_b16 v1, v74 offset:12544
	ds_write_b16 v1, v75 offset:13328
	ds_write_b16 v1, v76 offset:14112
	ds_write_b16 v1, v77 offset:14896
	s_cmpk_gt_u32 s49, 0xff
	s_cbranch_scc1 .Lf_wo_done
	s_waitcnt vmcnt(0)
	v_cvt_f16_f32_e32 v2, v102
	v_cvt_f16_f32_e32 v5, v105
	v_cvt_pk_f16_f32 v3, v103, v104
	v_pack_b32_f16 v2, v2, v3
	v_alignbit_b32 v3, v5, v3, 16
	v_and_b32_e32 v6, 0xff, v0
	v_lshlrev_b32_e32 v6, 3, v6
	s_lshl_b32 s22, s42, 1
	v_add_u32_e32 v6, s22, v6
	global_store_dwordx2 v6, v[2:3], s[18:19]
